# v42 plus expert-up act tile written with 16-byte write-through stores (row groups paired through ds_swizzle), half as many sc1 stores
# baseline (speedup 1.0000x reference)
.LBB0_1232:
	s_add_u32 s58, s2, 0xffffff00
	s_addc_u32 s59, s49, -1
	s_lshl_b32 s2, s43, 2
	s_add_i32 s2, s2, 0
	s_add_i32 s2, s2, 0x24080
	v_mov_b32_e32 v42, v131
	v_mov_b32_e32 v43, s2
	ds_read_b32 v43, v43
	v_mbcnt_lo_u32_b32 v42, -1, v42
	s_lshl_b32 s2, s69, 8
	v_mbcnt_hi_u32_b32 v42, -1, v42
	s_add_i32 s2, s2, s78
	v_ashrrev_i32_e32 v44, 1, v42
	v_and_or_b32 v42, v42, 15, s2
	s_lshl_b32 s34, s26, 7
	s_waitcnt lgkmcnt(0)
	v_add_u32_e32 v136, v42, v43
	v_and_b32_e32 v44, -8, v44
	s_or_b32 s34, s34, s5
	v_add_u32_e32 v134, s34, v44
	v_ashrrev_i32_e32 v137, 31, v136
	v_ashrrev_i32_e32 v135, 31, v134
	s_mov_b64 s[34:35], 0x8000
	s_and_b64 vcc, exec, s[8:9]
	v_lshlrev_b64 v[44:45], 11, v[136:137]
	v_lshl_add_u64 v[44:45], s[16:17], 0, v[44:45]
	v_lshl_add_u64 v[134:135], v[44:45], 0, v[134:135]
	v_mov_b32_e32 v50, 0x43800000
	v_mov_b32_e32 v51, 0x43800000
	v_min_f32_e32 v94, 0x44e00000, v94
	v_min_f32_e32 v95, 0x44e00000, v95
	v_min_f32_e32 v96, 0x44e00000, v96
	v_min_f32_e32 v97, 0x44e00000, v97
	v_pk_mul_f32 v[46:47], v[94:95], s[100:101] op_sel_hi:[1,0]
	v_pk_mul_f32 v[48:49], v[96:97], s[100:101] op_sel_hi:[1,0]
	v_exp_f32_e32 v46, v46
	v_exp_f32_e32 v47, v47
	v_exp_f32_e32 v48, v48
	v_exp_f32_e32 v49, v49
	v_med3_f32 v62, v62, s82, v139
	v_med3_f32 v63, v63, s82, v139
	v_med3_f32 v64, v64, s82, v139
	v_med3_f32 v65, v65, s82, v139
	v_pk_add_f32 v[62:63], v[62:63], v[50:51]
	v_pk_add_f32 v[64:65], v[64:65], v[50:51]
	v_pk_add_f32 v[46:47], v[46:47], 1.0 op_sel_hi:[1,0]
	v_pk_add_f32 v[48:49], v[48:49], 1.0 op_sel_hi:[1,0]
	v_rcp_f32_e32 v46, v46
	v_rcp_f32_e32 v47, v47
	v_rcp_f32_e32 v48, v48
	v_rcp_f32_e32 v49, v49
	v_pk_mul_f32 v[94:95], v[94:95], s[100:101] op_sel:[0,1]
	v_pk_mul_f32 v[96:97], v[96:97], s[100:101] op_sel:[0,1]
	v_pk_mul_f32 v[94:95], v[94:95], v[46:47]
	v_pk_mul_f32 v[96:97], v[96:97], v[48:49]
	v_pk_mul_f32 v[94:95], v[94:95], v[62:63]
	v_pk_mul_f32 v[96:97], v[96:97], v[64:65]
	v_min_f32_e32 v90, 0x44e00000, v90
	v_min_f32_e32 v91, 0x44e00000, v91
	v_min_f32_e32 v92, 0x44e00000, v92
	v_min_f32_e32 v93, 0x44e00000, v93
	v_pk_mul_f32 v[46:47], v[90:91], s[100:101] op_sel_hi:[1,0]
	v_pk_mul_f32 v[48:49], v[92:93], s[100:101] op_sel_hi:[1,0]
	v_exp_f32_e32 v46, v46
	v_exp_f32_e32 v47, v47
	v_exp_f32_e32 v48, v48
	v_exp_f32_e32 v49, v49
	v_med3_f32 v58, v58, s82, v139
	v_med3_f32 v59, v59, s82, v139
	v_med3_f32 v60, v60, s82, v139
	v_med3_f32 v61, v61, s82, v139
	v_pk_add_f32 v[58:59], v[58:59], v[50:51]
	v_pk_add_f32 v[60:61], v[60:61], v[50:51]
	v_pk_add_f32 v[46:47], v[46:47], 1.0 op_sel_hi:[1,0]
	v_pk_add_f32 v[48:49], v[48:49], 1.0 op_sel_hi:[1,0]
	v_rcp_f32_e32 v46, v46
	v_rcp_f32_e32 v47, v47
	v_rcp_f32_e32 v48, v48
	v_rcp_f32_e32 v49, v49
	v_pk_mul_f32 v[90:91], v[90:91], s[100:101] op_sel:[0,1]
	v_pk_mul_f32 v[92:93], v[92:93], s[100:101] op_sel:[0,1]
	v_pk_mul_f32 v[90:91], v[90:91], v[46:47]
	v_pk_mul_f32 v[92:93], v[92:93], v[48:49]
	v_pk_mul_f32 v[90:91], v[90:91], v[58:59]
	v_pk_mul_f32 v[92:93], v[92:93], v[60:61]
	v_mov_b32_e32 v62, v131
	v_mov_b32_e32 v63, v131
	v_cvt_pk_fp8_f32 v62, v94, v95
	v_cvt_pk_fp8_f32 v63, v90, v91
	v_cvt_pk_fp8_f32 v62, v96, v97 op_sel:[0,0,1]
	v_cvt_pk_fp8_f32 v63, v92, v93 op_sel:[0,0,1]
	v_lshl_add_u64 v[44:45], v[134:135], 0, s[34:35]
	s_mov_b64 s[34:35], 0x10000
	v_min_f32_e32 v86, 0x44e00000, v86
	v_min_f32_e32 v87, 0x44e00000, v87
	v_min_f32_e32 v88, 0x44e00000, v88
	v_min_f32_e32 v89, 0x44e00000, v89
	v_pk_mul_f32 v[46:47], v[86:87], s[100:101] op_sel_hi:[1,0]
	v_pk_mul_f32 v[48:49], v[88:89], s[100:101] op_sel_hi:[1,0]
	v_exp_f32_e32 v46, v46
	v_exp_f32_e32 v47, v47
	v_exp_f32_e32 v48, v48
	v_exp_f32_e32 v49, v49
	v_med3_f32 v54, v54, s82, v139
	v_med3_f32 v55, v55, s82, v139
	v_med3_f32 v56, v56, s82, v139
	v_med3_f32 v57, v57, s82, v139
	v_pk_add_f32 v[54:55], v[54:55], v[50:51]
	v_pk_add_f32 v[56:57], v[56:57], v[50:51]
	v_pk_add_f32 v[46:47], v[46:47], 1.0 op_sel_hi:[1,0]
	v_pk_add_f32 v[48:49], v[48:49], 1.0 op_sel_hi:[1,0]
	v_rcp_f32_e32 v46, v46
	v_rcp_f32_e32 v47, v47
	v_rcp_f32_e32 v48, v48
	v_rcp_f32_e32 v49, v49
	v_pk_mul_f32 v[86:87], v[86:87], s[100:101] op_sel:[0,1]
	v_pk_mul_f32 v[88:89], v[88:89], s[100:101] op_sel:[0,1]
	v_pk_mul_f32 v[86:87], v[86:87], v[46:47]
	v_pk_mul_f32 v[88:89], v[88:89], v[48:49]
	v_pk_mul_f32 v[86:87], v[86:87], v[54:55]
	v_pk_mul_f32 v[88:89], v[88:89], v[56:57]
	v_min_f32_e32 v82, 0x44e00000, v82
	v_min_f32_e32 v83, 0x44e00000, v83
	v_min_f32_e32 v84, 0x44e00000, v84
	v_min_f32_e32 v85, 0x44e00000, v85
	v_pk_mul_f32 v[46:47], v[82:83], s[100:101] op_sel_hi:[1,0]
	v_pk_mul_f32 v[48:49], v[84:85], s[100:101] op_sel_hi:[1,0]
	v_exp_f32_e32 v46, v46
	v_exp_f32_e32 v47, v47
	v_exp_f32_e32 v48, v48
	v_exp_f32_e32 v49, v49
	v_med3_f32 v176, v176, s82, v139
	v_med3_f32 v177, v177, s82, v139
	v_med3_f32 v178, v178, s82, v139
	v_med3_f32 v179, v179, s82, v139
	v_pk_add_f32 v[176:177], v[176:177], v[50:51]
	v_pk_add_f32 v[178:179], v[178:179], v[50:51]
	v_pk_add_f32 v[46:47], v[46:47], 1.0 op_sel_hi:[1,0]
	v_pk_add_f32 v[48:49], v[48:49], 1.0 op_sel_hi:[1,0]
	v_rcp_f32_e32 v46, v46
	v_rcp_f32_e32 v47, v47
	v_rcp_f32_e32 v48, v48
	v_rcp_f32_e32 v49, v49
	v_pk_mul_f32 v[82:83], v[82:83], s[100:101] op_sel:[0,1]
	v_pk_mul_f32 v[84:85], v[84:85], s[100:101] op_sel:[0,1]
	v_pk_mul_f32 v[82:83], v[82:83], v[46:47]
	v_pk_mul_f32 v[84:85], v[84:85], v[48:49]
	v_pk_mul_f32 v[82:83], v[82:83], v[176:177]
	v_pk_mul_f32 v[84:85], v[84:85], v[178:179]
	v_mov_b32_e32 v64, v131
	v_mov_b32_e32 v65, v131
	v_cvt_pk_fp8_f32 v64, v86, v87
	v_cvt_pk_fp8_f32 v65, v82, v83
	v_cvt_pk_fp8_f32 v64, v88, v89 op_sel:[0,0,1]
	v_cvt_pk_fp8_f32 v65, v84, v85 op_sel:[0,0,1]
	v_mbcnt_lo_u32_b32 v60, -1, 0
	v_mbcnt_hi_u32_b32 v60, -1, v60
	v_bfe_i32 v61, v60, 4, 1
	v_bfi_b32 v58, v61, v62, v64
	v_bfi_b32 v59, v61, v63, v65
	ds_swizzle_b32 v58, v58 offset:swizzle(SWAP,16)
	ds_swizzle_b32 v59, v59 offset:swizzle(SWAP,16)
	v_and_b32_e32 v86, 0x7ff8, v61
	v_add_u32_e32 v86, 0xffff8000, v86
	v_mov_b32_e32 v87, -1
	v_lshl_add_u64 v[88:89], v[86:87], 0, v[44:45]
	s_waitcnt lgkmcnt(0)
	v_bfi_b32 v94, v61, v58, v62
	v_bfi_b32 v95, v61, v59, v63
	v_bfi_b32 v96, v61, v64, v58
	v_bfi_b32 v97, v61, v65, v59
	global_store_dwordx4 v[88:89], v[94:97], off sc1
	s_nop 1
	v_lshl_add_u64 v[44:45], v[134:135], 0, s[34:35]
	s_mov_b64 s[34:35], 0x18000
	v_min_f32_e32 v78, 0x44e00000, v78
	v_min_f32_e32 v79, 0x44e00000, v79
	v_min_f32_e32 v80, 0x44e00000, v80
	v_min_f32_e32 v81, 0x44e00000, v81
	v_pk_mul_f32 v[46:47], v[78:79], s[100:101] op_sel_hi:[1,0]
	v_pk_mul_f32 v[48:49], v[80:81], s[100:101] op_sel_hi:[1,0]
	v_exp_f32_e32 v46, v46
	v_exp_f32_e32 v47, v47
	v_exp_f32_e32 v48, v48
	v_exp_f32_e32 v49, v49
	v_med3_f32 v172, v172, s82, v139
	v_med3_f32 v173, v173, s82, v139
	v_med3_f32 v174, v174, s82, v139
	v_med3_f32 v175, v175, s82, v139
	v_pk_add_f32 v[172:173], v[172:173], v[50:51]
	v_pk_add_f32 v[174:175], v[174:175], v[50:51]
	v_pk_add_f32 v[46:47], v[46:47], 1.0 op_sel_hi:[1,0]
	v_pk_add_f32 v[48:49], v[48:49], 1.0 op_sel_hi:[1,0]
	v_rcp_f32_e32 v46, v46
	v_rcp_f32_e32 v47, v47
	v_rcp_f32_e32 v48, v48
	v_rcp_f32_e32 v49, v49
	v_pk_mul_f32 v[78:79], v[78:79], s[100:101] op_sel:[0,1]
	v_pk_mul_f32 v[80:81], v[80:81], s[100:101] op_sel:[0,1]
	v_pk_mul_f32 v[78:79], v[78:79], v[46:47]
	v_pk_mul_f32 v[80:81], v[80:81], v[48:49]
	v_pk_mul_f32 v[78:79], v[78:79], v[172:173]
	v_pk_mul_f32 v[80:81], v[80:81], v[174:175]
	v_min_f32_e32 v74, 0x44e00000, v74
	v_min_f32_e32 v75, 0x44e00000, v75
	v_min_f32_e32 v76, 0x44e00000, v76
	v_min_f32_e32 v77, 0x44e00000, v77
	v_pk_mul_f32 v[46:47], v[74:75], s[100:101] op_sel_hi:[1,0]
	v_pk_mul_f32 v[48:49], v[76:77], s[100:101] op_sel_hi:[1,0]
	v_exp_f32_e32 v46, v46
	v_exp_f32_e32 v47, v47
	v_exp_f32_e32 v48, v48
	v_exp_f32_e32 v49, v49
	v_med3_f32 v18, v18, s82, v139
	v_med3_f32 v19, v19, s82, v139
	v_med3_f32 v20, v20, s82, v139
	v_med3_f32 v21, v21, s82, v139
	v_pk_add_f32 v[18:19], v[18:19], v[50:51]
	v_pk_add_f32 v[20:21], v[20:21], v[50:51]
	v_pk_add_f32 v[46:47], v[46:47], 1.0 op_sel_hi:[1,0]
	v_pk_add_f32 v[48:49], v[48:49], 1.0 op_sel_hi:[1,0]
	v_rcp_f32_e32 v46, v46
	v_rcp_f32_e32 v47, v47
	v_rcp_f32_e32 v48, v48
	v_rcp_f32_e32 v49, v49
	v_pk_mul_f32 v[74:75], v[74:75], s[100:101] op_sel:[0,1]
	v_pk_mul_f32 v[76:77], v[76:77], s[100:101] op_sel:[0,1]
	v_pk_mul_f32 v[74:75], v[74:75], v[46:47]
	v_pk_mul_f32 v[76:77], v[76:77], v[48:49]
	v_pk_mul_f32 v[74:75], v[74:75], v[18:19]
	v_pk_mul_f32 v[76:77], v[76:77], v[20:21]
	v_mov_b32_e32 v172, v131
	v_mov_b32_e32 v173, v131
	v_cvt_pk_fp8_f32 v172, v78, v79
	v_cvt_pk_fp8_f32 v173, v74, v75
	v_cvt_pk_fp8_f32 v172, v80, v81 op_sel:[0,0,1]
	v_cvt_pk_fp8_f32 v173, v76, v77 op_sel:[0,0,1]
	v_lshl_add_u64 v[44:45], v[134:135], 0, s[34:35]
	s_mov_b64 s[34:35], 0x48000
	v_min_f32_e32 v70, 0x44e00000, v70
	v_min_f32_e32 v71, 0x44e00000, v71
	v_min_f32_e32 v72, 0x44e00000, v72
	v_min_f32_e32 v73, 0x44e00000, v73
	v_pk_mul_f32 v[46:47], v[70:71], s[100:101] op_sel_hi:[1,0]
	v_pk_mul_f32 v[48:49], v[72:73], s[100:101] op_sel_hi:[1,0]
	v_exp_f32_e32 v46, v46
	v_exp_f32_e32 v47, v47
	v_exp_f32_e32 v48, v48
	v_exp_f32_e32 v49, v49
	v_med3_f32 v6, v6, s82, v139
	v_med3_f32 v7, v7, s82, v139
	v_med3_f32 v8, v8, s82, v139
	v_med3_f32 v9, v9, s82, v139
	v_pk_add_f32 v[6:7], v[6:7], v[50:51]
	v_pk_add_f32 v[8:9], v[8:9], v[50:51]
	v_pk_add_f32 v[46:47], v[46:47], 1.0 op_sel_hi:[1,0]
	v_pk_add_f32 v[48:49], v[48:49], 1.0 op_sel_hi:[1,0]
	v_rcp_f32_e32 v46, v46
	v_rcp_f32_e32 v47, v47
	v_rcp_f32_e32 v48, v48
	v_rcp_f32_e32 v49, v49
	v_pk_mul_f32 v[70:71], v[70:71], s[100:101] op_sel:[0,1]
	v_pk_mul_f32 v[72:73], v[72:73], s[100:101] op_sel:[0,1]
	v_pk_mul_f32 v[70:71], v[70:71], v[46:47]
	v_pk_mul_f32 v[72:73], v[72:73], v[48:49]
	v_pk_mul_f32 v[70:71], v[70:71], v[6:7]
	v_pk_mul_f32 v[72:73], v[72:73], v[8:9]
	v_min_f32_e32 v66, 0x44e00000, v66
	v_min_f32_e32 v67, 0x44e00000, v67
	v_min_f32_e32 v68, 0x44e00000, v68
	v_min_f32_e32 v69, 0x44e00000, v69
	v_pk_mul_f32 v[46:47], v[66:67], s[100:101] op_sel_hi:[1,0]
	v_pk_mul_f32 v[48:49], v[68:69], s[100:101] op_sel_hi:[1,0]
	v_exp_f32_e32 v46, v46
	v_exp_f32_e32 v47, v47
	v_exp_f32_e32 v48, v48
	v_exp_f32_e32 v49, v49
	v_med3_f32 v14, v14, s82, v139
	v_med3_f32 v15, v15, s82, v139
	v_med3_f32 v16, v16, s82, v139
	v_med3_f32 v17, v17, s82, v139
	v_pk_add_f32 v[14:15], v[14:15], v[50:51]
	v_pk_add_f32 v[16:17], v[16:17], v[50:51]
	v_pk_add_f32 v[46:47], v[46:47], 1.0 op_sel_hi:[1,0]
	v_pk_add_f32 v[48:49], v[48:49], 1.0 op_sel_hi:[1,0]
	v_rcp_f32_e32 v46, v46
	v_rcp_f32_e32 v47, v47
	v_rcp_f32_e32 v48, v48
	v_rcp_f32_e32 v49, v49
	v_pk_mul_f32 v[66:67], v[66:67], s[100:101] op_sel:[0,1]
	v_pk_mul_f32 v[68:69], v[68:69], s[100:101] op_sel:[0,1]
	v_pk_mul_f32 v[66:67], v[66:67], v[46:47]
	v_pk_mul_f32 v[68:69], v[68:69], v[48:49]
	v_pk_mul_f32 v[66:67], v[66:67], v[14:15]
	v_pk_mul_f32 v[68:69], v[68:69], v[16:17]
	v_mov_b32_e32 v174, v131
	v_mov_b32_e32 v175, v131
	v_cvt_pk_fp8_f32 v174, v70, v71
	v_cvt_pk_fp8_f32 v175, v66, v67
	v_cvt_pk_fp8_f32 v174, v72, v73 op_sel:[0,0,1]
	v_cvt_pk_fp8_f32 v175, v68, v69 op_sel:[0,0,1]
	v_mbcnt_lo_u32_b32 v20, -1, 0
	v_mbcnt_hi_u32_b32 v20, -1, v20
	v_bfe_i32 v21, v20, 4, 1
	v_bfi_b32 v18, v21, v172, v174
	v_bfi_b32 v19, v21, v173, v175
	ds_swizzle_b32 v18, v18 offset:swizzle(SWAP,16)
	ds_swizzle_b32 v19, v19 offset:swizzle(SWAP,16)
	v_and_b32_e32 v70, 0x7ff8, v21
	v_add_u32_e32 v70, 0xffff8000, v70
	v_mov_b32_e32 v71, -1
	v_lshl_add_u64 v[72:73], v[70:71], 0, v[44:45]
	s_waitcnt lgkmcnt(0)
	v_bfi_b32 v78, v21, v18, v172
	v_bfi_b32 v79, v21, v19, v173
	v_bfi_b32 v80, v21, v174, v18
	v_bfi_b32 v81, v21, v175, v19
	global_store_dwordx4 v[72:73], v[78:81], off sc1
	s_nop 1
	v_lshl_add_u64 v[44:45], v[134:135], 0, s[22:23]
	v_min_f32_e32 v38, 0x44e00000, v38
	v_min_f32_e32 v39, 0x44e00000, v39
	v_min_f32_e32 v40, 0x44e00000, v40
	v_min_f32_e32 v41, 0x44e00000, v41
	v_pk_mul_f32 v[46:47], v[38:39], s[100:101] op_sel_hi:[1,0]
	v_pk_mul_f32 v[48:49], v[40:41], s[100:101] op_sel_hi:[1,0]
	v_exp_f32_e32 v46, v46
	v_exp_f32_e32 v47, v47
	v_exp_f32_e32 v48, v48
	v_exp_f32_e32 v49, v49
	v_med3_f32 v98, v98, s82, v139
	v_med3_f32 v99, v99, s82, v139
	v_med3_f32 v100, v100, s82, v139
	v_med3_f32 v101, v101, s82, v139
	v_pk_add_f32 v[98:99], v[98:99], v[50:51]
	v_pk_add_f32 v[100:101], v[100:101], v[50:51]
	v_pk_add_f32 v[46:47], v[46:47], 1.0 op_sel_hi:[1,0]
	v_pk_add_f32 v[48:49], v[48:49], 1.0 op_sel_hi:[1,0]
	v_rcp_f32_e32 v46, v46
	v_rcp_f32_e32 v47, v47
	v_rcp_f32_e32 v48, v48
	v_rcp_f32_e32 v49, v49
	v_pk_mul_f32 v[38:39], v[38:39], s[100:101] op_sel:[0,1]
	v_pk_mul_f32 v[40:41], v[40:41], s[100:101] op_sel:[0,1]
	v_pk_mul_f32 v[38:39], v[38:39], v[46:47]
	v_pk_mul_f32 v[40:41], v[40:41], v[48:49]
	v_pk_mul_f32 v[38:39], v[38:39], v[98:99]
	v_pk_mul_f32 v[40:41], v[40:41], v[100:101]
	v_min_f32_e32 v34, 0x44e00000, v34
	v_min_f32_e32 v35, 0x44e00000, v35
	v_min_f32_e32 v36, 0x44e00000, v36
	v_min_f32_e32 v37, 0x44e00000, v37
	v_pk_mul_f32 v[46:47], v[34:35], s[100:101] op_sel_hi:[1,0]
	v_pk_mul_f32 v[48:49], v[36:37], s[100:101] op_sel_hi:[1,0]
	v_exp_f32_e32 v46, v46
	v_exp_f32_e32 v47, v47
	v_exp_f32_e32 v48, v48
	v_exp_f32_e32 v49, v49
	v_med3_f32 v102, v102, s82, v139
	v_med3_f32 v103, v103, s82, v139
	v_med3_f32 v104, v104, s82, v139
	v_med3_f32 v105, v105, s82, v139
	v_pk_add_f32 v[102:103], v[102:103], v[50:51]
	v_pk_add_f32 v[104:105], v[104:105], v[50:51]
	v_pk_add_f32 v[46:47], v[46:47], 1.0 op_sel_hi:[1,0]
	v_pk_add_f32 v[48:49], v[48:49], 1.0 op_sel_hi:[1,0]
	v_rcp_f32_e32 v46, v46
	v_rcp_f32_e32 v47, v47
	v_rcp_f32_e32 v48, v48
	v_rcp_f32_e32 v49, v49
	v_pk_mul_f32 v[34:35], v[34:35], s[100:101] op_sel:[0,1]
	v_pk_mul_f32 v[36:37], v[36:37], s[100:101] op_sel:[0,1]
	v_pk_mul_f32 v[34:35], v[34:35], v[46:47]
	v_pk_mul_f32 v[36:37], v[36:37], v[48:49]
	v_pk_mul_f32 v[34:35], v[34:35], v[102:103]
	v_pk_mul_f32 v[36:37], v[36:37], v[104:105]
	v_mov_b32_e32 v98, v131
	v_mov_b32_e32 v99, v131
	v_cvt_pk_fp8_f32 v98, v38, v39
	v_cvt_pk_fp8_f32 v99, v34, v35
	v_cvt_pk_fp8_f32 v98, v40, v41 op_sel:[0,0,1]
	v_cvt_pk_fp8_f32 v99, v36, v37 op_sel:[0,0,1]
	v_lshl_add_u64 v[44:45], v[134:135], 0, s[34:35]
	s_mov_b64 s[34:35], 0x50000
	v_min_f32_e32 v30, 0x44e00000, v30
	v_min_f32_e32 v31, 0x44e00000, v31
	v_min_f32_e32 v32, 0x44e00000, v32
	v_min_f32_e32 v33, 0x44e00000, v33
	v_pk_mul_f32 v[46:47], v[30:31], s[100:101] op_sel_hi:[1,0]
	v_pk_mul_f32 v[48:49], v[32:33], s[100:101] op_sel_hi:[1,0]
	v_exp_f32_e32 v46, v46
	v_exp_f32_e32 v47, v47
	v_exp_f32_e32 v48, v48
	v_exp_f32_e32 v49, v49
	v_med3_f32 v106, v106, s82, v139
	v_med3_f32 v107, v107, s82, v139
	v_med3_f32 v108, v108, s82, v139
	v_med3_f32 v109, v109, s82, v139
	v_pk_add_f32 v[106:107], v[106:107], v[50:51]
	v_pk_add_f32 v[108:109], v[108:109], v[50:51]
	v_pk_add_f32 v[46:47], v[46:47], 1.0 op_sel_hi:[1,0]
	v_pk_add_f32 v[48:49], v[48:49], 1.0 op_sel_hi:[1,0]
	v_rcp_f32_e32 v46, v46
	v_rcp_f32_e32 v47, v47
	v_rcp_f32_e32 v48, v48
	v_rcp_f32_e32 v49, v49
	v_pk_mul_f32 v[30:31], v[30:31], s[100:101] op_sel:[0,1]
	v_pk_mul_f32 v[32:33], v[32:33], s[100:101] op_sel:[0,1]
	v_pk_mul_f32 v[30:31], v[30:31], v[46:47]
	v_pk_mul_f32 v[32:33], v[32:33], v[48:49]
	v_pk_mul_f32 v[30:31], v[30:31], v[106:107]
	v_pk_mul_f32 v[32:33], v[32:33], v[108:109]
	v_min_f32_e32 v26, 0x44e00000, v26
	v_min_f32_e32 v27, 0x44e00000, v27
	v_min_f32_e32 v28, 0x44e00000, v28
	v_min_f32_e32 v29, 0x44e00000, v29
	v_pk_mul_f32 v[46:47], v[26:27], s[100:101] op_sel_hi:[1,0]
	v_pk_mul_f32 v[48:49], v[28:29], s[100:101] op_sel_hi:[1,0]
	v_exp_f32_e32 v46, v46
	v_exp_f32_e32 v47, v47
	v_exp_f32_e32 v48, v48
	v_exp_f32_e32 v49, v49
	v_med3_f32 v110, v110, s82, v139
	v_med3_f32 v111, v111, s82, v139
	v_med3_f32 v112, v112, s82, v139
	v_med3_f32 v113, v113, s82, v139
	v_pk_add_f32 v[110:111], v[110:111], v[50:51]
	v_pk_add_f32 v[112:113], v[112:113], v[50:51]
	v_pk_add_f32 v[46:47], v[46:47], 1.0 op_sel_hi:[1,0]
	v_pk_add_f32 v[48:49], v[48:49], 1.0 op_sel_hi:[1,0]
	v_rcp_f32_e32 v46, v46
	v_rcp_f32_e32 v47, v47
	v_rcp_f32_e32 v48, v48
	v_rcp_f32_e32 v49, v49
	v_pk_mul_f32 v[26:27], v[26:27], s[100:101] op_sel:[0,1]
	v_pk_mul_f32 v[28:29], v[28:29], s[100:101] op_sel:[0,1]
	v_pk_mul_f32 v[26:27], v[26:27], v[46:47]
	v_pk_mul_f32 v[28:29], v[28:29], v[48:49]
	v_pk_mul_f32 v[26:27], v[26:27], v[110:111]
	v_pk_mul_f32 v[28:29], v[28:29], v[112:113]
	v_mov_b32_e32 v100, v131
	v_mov_b32_e32 v101, v131
	v_cvt_pk_fp8_f32 v100, v30, v31
	v_cvt_pk_fp8_f32 v101, v26, v27
	v_cvt_pk_fp8_f32 v100, v32, v33 op_sel:[0,0,1]
	v_cvt_pk_fp8_f32 v101, v28, v29 op_sel:[0,0,1]
	v_mbcnt_lo_u32_b32 v104, -1, 0
	v_mbcnt_hi_u32_b32 v104, -1, v104
	v_bfe_i32 v105, v104, 4, 1
	v_bfi_b32 v102, v105, v98, v100
	v_bfi_b32 v103, v105, v99, v101
	ds_swizzle_b32 v102, v102 offset:swizzle(SWAP,16)
	ds_swizzle_b32 v103, v103 offset:swizzle(SWAP,16)
	v_and_b32_e32 v30, 0x7ff8, v105
	v_add_u32_e32 v30, 0xffff8000, v30
	v_mov_b32_e32 v31, -1
	v_lshl_add_u64 v[32:33], v[30:31], 0, v[44:45]
	s_waitcnt lgkmcnt(0)
	v_bfi_b32 v38, v105, v102, v98
	v_bfi_b32 v39, v105, v103, v99
	v_bfi_b32 v40, v105, v100, v102
	v_bfi_b32 v41, v105, v101, v103
	global_store_dwordx4 v[32:33], v[38:41], off sc1
	s_nop 1
	v_lshl_add_u64 v[44:45], v[134:135], 0, s[34:35]
	s_mov_b64 s[34:35], 0x58000
	v_min_f32_e32 v22, 0x44e00000, v22
	v_min_f32_e32 v23, 0x44e00000, v23
	v_min_f32_e32 v24, 0x44e00000, v24
	v_min_f32_e32 v25, 0x44e00000, v25
	v_pk_mul_f32 v[46:47], v[22:23], s[100:101] op_sel_hi:[1,0]
	v_pk_mul_f32 v[48:49], v[24:25], s[100:101] op_sel_hi:[1,0]
	v_exp_f32_e32 v46, v46
	v_exp_f32_e32 v47, v47
	v_exp_f32_e32 v48, v48
	v_exp_f32_e32 v49, v49
	v_med3_f32 v114, v114, s82, v139
	v_med3_f32 v115, v115, s82, v139
	v_med3_f32 v116, v116, s82, v139
	v_med3_f32 v117, v117, s82, v139
	v_pk_add_f32 v[114:115], v[114:115], v[50:51]
	v_pk_add_f32 v[116:117], v[116:117], v[50:51]
	v_pk_add_f32 v[46:47], v[46:47], 1.0 op_sel_hi:[1,0]
	v_pk_add_f32 v[48:49], v[48:49], 1.0 op_sel_hi:[1,0]
	v_rcp_f32_e32 v46, v46
	v_rcp_f32_e32 v47, v47
	v_rcp_f32_e32 v48, v48
	v_rcp_f32_e32 v49, v49
	v_pk_mul_f32 v[22:23], v[22:23], s[100:101] op_sel:[0,1]
	v_pk_mul_f32 v[24:25], v[24:25], s[100:101] op_sel:[0,1]
	v_pk_mul_f32 v[22:23], v[22:23], v[46:47]
	v_pk_mul_f32 v[24:25], v[24:25], v[48:49]
	v_pk_mul_f32 v[22:23], v[22:23], v[114:115]
	v_pk_mul_f32 v[24:25], v[24:25], v[116:117]
	v_min_f32_e32 v220, 0x44e00000, v220
	v_min_f32_e32 v221, 0x44e00000, v221
	v_min_f32_e32 v222, 0x44e00000, v222
	v_min_f32_e32 v223, 0x44e00000, v223
	v_pk_mul_f32 v[46:47], v[220:221], s[100:101] op_sel_hi:[1,0]
	v_pk_mul_f32 v[48:49], v[222:223], s[100:101] op_sel_hi:[1,0]
	v_exp_f32_e32 v46, v46
	v_exp_f32_e32 v47, v47
	v_exp_f32_e32 v48, v48
	v_exp_f32_e32 v49, v49
	v_med3_f32 v118, v118, s82, v139
	v_med3_f32 v119, v119, s82, v139
	v_med3_f32 v120, v120, s82, v139
	v_med3_f32 v121, v121, s82, v139
	v_pk_add_f32 v[118:119], v[118:119], v[50:51]
	v_pk_add_f32 v[120:121], v[120:121], v[50:51]
	v_pk_add_f32 v[46:47], v[46:47], 1.0 op_sel_hi:[1,0]
	v_pk_add_f32 v[48:49], v[48:49], 1.0 op_sel_hi:[1,0]
	v_rcp_f32_e32 v46, v46
	v_rcp_f32_e32 v47, v47
	v_rcp_f32_e32 v48, v48
	v_rcp_f32_e32 v49, v49
	v_pk_mul_f32 v[220:221], v[220:221], s[100:101] op_sel:[0,1]
	v_pk_mul_f32 v[222:223], v[222:223], s[100:101] op_sel:[0,1]
	v_pk_mul_f32 v[220:221], v[220:221], v[46:47]
	v_pk_mul_f32 v[222:223], v[222:223], v[48:49]
	v_pk_mul_f32 v[220:221], v[220:221], v[118:119]
	v_pk_mul_f32 v[222:223], v[222:223], v[120:121]
	v_mov_b32_e32 v114, v131
	v_mov_b32_e32 v115, v131
	v_cvt_pk_fp8_f32 v114, v22, v23
	v_cvt_pk_fp8_f32 v115, v220, v221
	v_cvt_pk_fp8_f32 v114, v24, v25 op_sel:[0,0,1]
	v_cvt_pk_fp8_f32 v115, v222, v223 op_sel:[0,0,1]
	v_lshl_add_u64 v[44:45], v[134:135], 0, s[34:35]
	v_min_f32_e32 v2, 0x44e00000, v2
	v_min_f32_e32 v3, 0x44e00000, v3
	v_min_f32_e32 v4, 0x44e00000, v4
	v_min_f32_e32 v5, 0x44e00000, v5
	v_pk_mul_f32 v[46:47], v[2:3], s[100:101] op_sel_hi:[1,0]
	v_pk_mul_f32 v[48:49], v[4:5], s[100:101] op_sel_hi:[1,0]
	v_exp_f32_e32 v46, v46
	v_exp_f32_e32 v47, v47
	v_exp_f32_e32 v48, v48
	v_exp_f32_e32 v49, v49
	v_med3_f32 v122, v122, s82, v139
	v_med3_f32 v123, v123, s82, v139
	v_med3_f32 v124, v124, s82, v139
	v_med3_f32 v125, v125, s82, v139
	v_pk_add_f32 v[122:123], v[122:123], v[50:51]
	v_pk_add_f32 v[124:125], v[124:125], v[50:51]
	v_pk_add_f32 v[46:47], v[46:47], 1.0 op_sel_hi:[1,0]
	v_pk_add_f32 v[48:49], v[48:49], 1.0 op_sel_hi:[1,0]
	v_rcp_f32_e32 v46, v46
	v_rcp_f32_e32 v47, v47
	v_rcp_f32_e32 v48, v48
	v_rcp_f32_e32 v49, v49
	v_pk_mul_f32 v[2:3], v[2:3], s[100:101] op_sel:[0,1]
	v_pk_mul_f32 v[4:5], v[4:5], s[100:101] op_sel:[0,1]
	v_pk_mul_f32 v[2:3], v[2:3], v[46:47]
	v_pk_mul_f32 v[4:5], v[4:5], v[48:49]
	v_pk_mul_f32 v[2:3], v[2:3], v[122:123]
	v_pk_mul_f32 v[4:5], v[4:5], v[124:125]
	v_min_f32_e32 v10, 0x44e00000, v10
	v_min_f32_e32 v11, 0x44e00000, v11
	v_min_f32_e32 v12, 0x44e00000, v12
	v_min_f32_e32 v13, 0x44e00000, v13
	v_pk_mul_f32 v[46:47], v[10:11], s[100:101] op_sel_hi:[1,0]
	v_pk_mul_f32 v[48:49], v[12:13], s[100:101] op_sel_hi:[1,0]
	v_exp_f32_e32 v46, v46
	v_exp_f32_e32 v47, v47
	v_exp_f32_e32 v48, v48
	v_exp_f32_e32 v49, v49
	v_med3_f32 v126, v126, s82, v139
	v_med3_f32 v127, v127, s82, v139
	v_med3_f32 v128, v128, s82, v139
	v_med3_f32 v129, v129, s82, v139
	v_pk_add_f32 v[126:127], v[126:127], v[50:51]
	v_pk_add_f32 v[128:129], v[128:129], v[50:51]
	v_pk_add_f32 v[46:47], v[46:47], 1.0 op_sel_hi:[1,0]
	v_pk_add_f32 v[48:49], v[48:49], 1.0 op_sel_hi:[1,0]
	v_rcp_f32_e32 v46, v46
	v_rcp_f32_e32 v47, v47
	v_rcp_f32_e32 v48, v48
	v_rcp_f32_e32 v49, v49
	v_pk_mul_f32 v[10:11], v[10:11], s[100:101] op_sel:[0,1]
	v_pk_mul_f32 v[12:13], v[12:13], s[100:101] op_sel:[0,1]
	v_pk_mul_f32 v[10:11], v[10:11], v[46:47]
	v_pk_mul_f32 v[12:13], v[12:13], v[48:49]
	v_pk_mul_f32 v[10:11], v[10:11], v[126:127]
	v_pk_mul_f32 v[12:13], v[12:13], v[128:129]
	v_mov_b32_e32 v116, v131
	v_mov_b32_e32 v117, v131
	v_cvt_pk_fp8_f32 v116, v2, v3
	v_cvt_pk_fp8_f32 v117, v10, v11
	v_cvt_pk_fp8_f32 v116, v4, v5 op_sel:[0,0,1]
	v_cvt_pk_fp8_f32 v117, v12, v13 op_sel:[0,0,1]
	v_mbcnt_lo_u32_b32 v120, -1, 0
	v_mbcnt_hi_u32_b32 v120, -1, v120
	v_bfe_i32 v121, v120, 4, 1
	v_bfi_b32 v118, v121, v114, v116
	v_bfi_b32 v119, v121, v115, v117
	ds_swizzle_b32 v118, v118 offset:swizzle(SWAP,16)
	ds_swizzle_b32 v119, v119 offset:swizzle(SWAP,16)
	v_and_b32_e32 v2, 0x7ff8, v121
	v_add_u32_e32 v2, 0xffff8000, v2
	v_mov_b32_e32 v3, -1
	v_lshl_add_u64 v[4:5], v[2:3], 0, v[44:45]
	s_waitcnt lgkmcnt(0)
	v_bfi_b32 v22, v121, v118, v114
	v_bfi_b32 v23, v121, v119, v115
	v_bfi_b32 v24, v121, v116, v118
	v_bfi_b32 v25, v121, v117, v119
	global_store_dwordx4 v[4:5], v[22:25], off sc1
	s_nop 1
	s_cbranch_vccnz .LBB0_1236
	s_ashr_i32 s49, s48, 31
	v_readlane_b32 s88, v254, 4
	s_lshl_b64 s[8:9], s[48:49], 14
	v_readlane_b32 s92, v254, 8
	v_readlane_b32 s93, v254, 9
	s_add_u32 s2, s92, s8
	v_mov_b32_e32 v2, v131
	s_addc_u32 s26, s93, s9
	s_lshl_b32 s8, s50, 7
	s_ashr_i32 s9, s8, 31
	v_mbcnt_lo_u32_b32 v2, -1, v2
	s_lshl_b64 s[8:9], s[8:9], 2
	v_mbcnt_hi_u32_b32 v2, -1, v2
	s_add_u32 s2, s2, s8
	s_addc_u32 s9, s26, s9
	s_lshl_b32 s8, s5, 2
	v_ashrrev_i32_e32 v2, 1, v2
	s_add_u32 s8, s2, s8
	v_and_b32_e32 v2, -8, v2
	s_addc_u32 s9, s9, 0
	v_ashrrev_i32_e32 v3, 31, v2
	v_lshl_add_u64 v[6:7], v[2:3], 2, s[8:9]
	v_lshl_add_u64 v[14:15], v[6:7], 0, s[18:19]
	global_load_dwordx4 v[10:13], v[6:7], off offset:16
	global_load_dwordx4 v[2:5], v[6:7], off
	v_add_co_u32_e32 v6, vcc, 0x2000, v6
	v_readlane_b32 s89, v254, 5
	s_nop 0
	v_addc_co_u32_e32 v7, vcc, 0, v7, vcc
	global_load_dwordx4 v[6:9], v[6:7], off
	s_nop 0
	global_load_dwordx4 v[14:17], v[14:15], off offset:16
	s_andn2_b64 vcc, exec, s[28:29]
	v_readlane_b32 s90, v254, 6
	v_readlane_b32 s91, v254, 7
	v_readlane_b32 s94, v254, 10
	v_readlane_b32 s95, v254, 11
	s_cbranch_vccnz .LBB0_1235
	s_barrier

.LBB0_1265:
	s_add_u32 s54, s45, 0xffffff00
	s_addc_u32 s55, s47, -1
	s_lshl_b32 s34, s64, 2
	s_add_i32 s34, s34, 0
	s_add_i32 s34, s34, 0x24080
	v_mov_b32_e32 v42, v131
	v_mov_b32_e32 v43, s34
	ds_read_b32 v43, v43
	v_mbcnt_lo_u32_b32 v42, -1, v42
	s_lshl_b32 s34, s65, 8
	v_mbcnt_hi_u32_b32 v42, -1, v42
	s_add_i32 s34, s34, s77
	v_ashrrev_i32_e32 v44, 1, v42
	v_and_or_b32 v42, v42, 15, s34
	s_lshl_b32 s35, s22, 7
	s_waitcnt lgkmcnt(0)
	v_add_u32_e32 v136, v42, v43
	v_and_b32_e32 v44, -8, v44
	s_or_b32 s35, s35, s63
	v_add_u32_e32 v134, s35, v44
	v_ashrrev_i32_e32 v137, 31, v136
	v_ashrrev_i32_e32 v135, 31, v134
	s_mov_b64 s[34:35], 0x8000
	s_and_b64 vcc, exec, s[4:5]
	v_lshlrev_b64 v[44:45], 11, v[136:137]
	v_lshl_add_u64 v[44:45], s[16:17], 0, v[44:45]
	v_lshl_add_u64 v[134:135], v[44:45], 0, v[134:135]
	v_mov_b32_e32 v50, 0x43800000
	v_mov_b32_e32 v51, 0x43800000
	v_min_f32_e32 v94, 0x44e00000, v94
	v_min_f32_e32 v95, 0x44e00000, v95
	v_min_f32_e32 v96, 0x44e00000, v96
	v_min_f32_e32 v97, 0x44e00000, v97
	v_pk_mul_f32 v[46:47], v[94:95], s[100:101] op_sel_hi:[1,0]
	v_pk_mul_f32 v[48:49], v[96:97], s[100:101] op_sel_hi:[1,0]
	v_exp_f32_e32 v46, v46
	v_exp_f32_e32 v47, v47
	v_exp_f32_e32 v48, v48
	v_exp_f32_e32 v49, v49
	v_med3_f32 v62, v62, s81, v139
	v_med3_f32 v63, v63, s81, v139
	v_med3_f32 v64, v64, s81, v139
	v_med3_f32 v65, v65, s81, v139
	v_pk_add_f32 v[62:63], v[62:63], v[50:51]
	v_pk_add_f32 v[64:65], v[64:65], v[50:51]
	v_pk_add_f32 v[46:47], v[46:47], 1.0 op_sel_hi:[1,0]
	v_pk_add_f32 v[48:49], v[48:49], 1.0 op_sel_hi:[1,0]
	v_rcp_f32_e32 v46, v46
	v_rcp_f32_e32 v47, v47
	v_rcp_f32_e32 v48, v48
	v_rcp_f32_e32 v49, v49
	v_pk_mul_f32 v[94:95], v[94:95], s[100:101] op_sel:[0,1]
	v_pk_mul_f32 v[96:97], v[96:97], s[100:101] op_sel:[0,1]
	v_pk_mul_f32 v[94:95], v[94:95], v[46:47]
	v_pk_mul_f32 v[96:97], v[96:97], v[48:49]
	v_pk_mul_f32 v[94:95], v[94:95], v[62:63]
	v_pk_mul_f32 v[96:97], v[96:97], v[64:65]
	v_min_f32_e32 v90, 0x44e00000, v90
	v_min_f32_e32 v91, 0x44e00000, v91
	v_min_f32_e32 v92, 0x44e00000, v92
	v_min_f32_e32 v93, 0x44e00000, v93
	v_pk_mul_f32 v[46:47], v[90:91], s[100:101] op_sel_hi:[1,0]
	v_pk_mul_f32 v[48:49], v[92:93], s[100:101] op_sel_hi:[1,0]
	v_exp_f32_e32 v46, v46
	v_exp_f32_e32 v47, v47
	v_exp_f32_e32 v48, v48
	v_exp_f32_e32 v49, v49
	v_med3_f32 v58, v58, s81, v139
	v_med3_f32 v59, v59, s81, v139
	v_med3_f32 v60, v60, s81, v139
	v_med3_f32 v61, v61, s81, v139
	v_pk_add_f32 v[58:59], v[58:59], v[50:51]
	v_pk_add_f32 v[60:61], v[60:61], v[50:51]
	v_pk_add_f32 v[46:47], v[46:47], 1.0 op_sel_hi:[1,0]
	v_pk_add_f32 v[48:49], v[48:49], 1.0 op_sel_hi:[1,0]
	v_rcp_f32_e32 v46, v46
	v_rcp_f32_e32 v47, v47
	v_rcp_f32_e32 v48, v48
	v_rcp_f32_e32 v49, v49
	v_pk_mul_f32 v[90:91], v[90:91], s[100:101] op_sel:[0,1]
	v_pk_mul_f32 v[92:93], v[92:93], s[100:101] op_sel:[0,1]
	v_pk_mul_f32 v[90:91], v[90:91], v[46:47]
	v_pk_mul_f32 v[92:93], v[92:93], v[48:49]
	v_pk_mul_f32 v[90:91], v[90:91], v[58:59]
	v_pk_mul_f32 v[92:93], v[92:93], v[60:61]
	v_mov_b32_e32 v62, v131
	v_mov_b32_e32 v63, v131
	v_cvt_pk_fp8_f32 v62, v94, v95
	v_cvt_pk_fp8_f32 v63, v90, v91
	v_cvt_pk_fp8_f32 v62, v96, v97 op_sel:[0,0,1]
	v_cvt_pk_fp8_f32 v63, v92, v93 op_sel:[0,0,1]
	v_lshl_add_u64 v[44:45], v[134:135], 0, s[34:35]
	s_mov_b64 s[34:35], 0x10000
	v_min_f32_e32 v86, 0x44e00000, v86
	v_min_f32_e32 v87, 0x44e00000, v87
	v_min_f32_e32 v88, 0x44e00000, v88
	v_min_f32_e32 v89, 0x44e00000, v89
	v_pk_mul_f32 v[46:47], v[86:87], s[100:101] op_sel_hi:[1,0]
	v_pk_mul_f32 v[48:49], v[88:89], s[100:101] op_sel_hi:[1,0]
	v_exp_f32_e32 v46, v46
	v_exp_f32_e32 v47, v47
	v_exp_f32_e32 v48, v48
	v_exp_f32_e32 v49, v49
	v_med3_f32 v54, v54, s81, v139
	v_med3_f32 v55, v55, s81, v139
	v_med3_f32 v56, v56, s81, v139
	v_med3_f32 v57, v57, s81, v139
	v_pk_add_f32 v[54:55], v[54:55], v[50:51]
	v_pk_add_f32 v[56:57], v[56:57], v[50:51]
	v_pk_add_f32 v[46:47], v[46:47], 1.0 op_sel_hi:[1,0]
	v_pk_add_f32 v[48:49], v[48:49], 1.0 op_sel_hi:[1,0]
	v_rcp_f32_e32 v46, v46
	v_rcp_f32_e32 v47, v47
	v_rcp_f32_e32 v48, v48
	v_rcp_f32_e32 v49, v49
	v_pk_mul_f32 v[86:87], v[86:87], s[100:101] op_sel:[0,1]
	v_pk_mul_f32 v[88:89], v[88:89], s[100:101] op_sel:[0,1]
	v_pk_mul_f32 v[86:87], v[86:87], v[46:47]
	v_pk_mul_f32 v[88:89], v[88:89], v[48:49]
	v_pk_mul_f32 v[86:87], v[86:87], v[54:55]
	v_pk_mul_f32 v[88:89], v[88:89], v[56:57]
	v_min_f32_e32 v82, 0x44e00000, v82
	v_min_f32_e32 v83, 0x44e00000, v83
	v_min_f32_e32 v84, 0x44e00000, v84
	v_min_f32_e32 v85, 0x44e00000, v85
	v_pk_mul_f32 v[46:47], v[82:83], s[100:101] op_sel_hi:[1,0]
	v_pk_mul_f32 v[48:49], v[84:85], s[100:101] op_sel_hi:[1,0]
	v_exp_f32_e32 v46, v46
	v_exp_f32_e32 v47, v47
	v_exp_f32_e32 v48, v48
	v_exp_f32_e32 v49, v49
	v_med3_f32 v176, v176, s81, v139
	v_med3_f32 v177, v177, s81, v139
	v_med3_f32 v178, v178, s81, v139
	v_med3_f32 v179, v179, s81, v139
	v_pk_add_f32 v[176:177], v[176:177], v[50:51]
	v_pk_add_f32 v[178:179], v[178:179], v[50:51]
	v_pk_add_f32 v[46:47], v[46:47], 1.0 op_sel_hi:[1,0]
	v_pk_add_f32 v[48:49], v[48:49], 1.0 op_sel_hi:[1,0]
	v_rcp_f32_e32 v46, v46
	v_rcp_f32_e32 v47, v47
	v_rcp_f32_e32 v48, v48
	v_rcp_f32_e32 v49, v49
	v_pk_mul_f32 v[82:83], v[82:83], s[100:101] op_sel:[0,1]
	v_pk_mul_f32 v[84:85], v[84:85], s[100:101] op_sel:[0,1]
	v_pk_mul_f32 v[82:83], v[82:83], v[46:47]
	v_pk_mul_f32 v[84:85], v[84:85], v[48:49]
	v_pk_mul_f32 v[82:83], v[82:83], v[176:177]
	v_pk_mul_f32 v[84:85], v[84:85], v[178:179]
	v_mov_b32_e32 v64, v131
	v_mov_b32_e32 v65, v131
	v_cvt_pk_fp8_f32 v64, v86, v87
	v_cvt_pk_fp8_f32 v65, v82, v83
	v_cvt_pk_fp8_f32 v64, v88, v89 op_sel:[0,0,1]
	v_cvt_pk_fp8_f32 v65, v84, v85 op_sel:[0,0,1]
	v_mbcnt_lo_u32_b32 v60, -1, 0
	v_mbcnt_hi_u32_b32 v60, -1, v60
	v_bfe_i32 v61, v60, 4, 1
	v_bfi_b32 v58, v61, v62, v64
	v_bfi_b32 v59, v61, v63, v65
	ds_swizzle_b32 v58, v58 offset:swizzle(SWAP,16)
	ds_swizzle_b32 v59, v59 offset:swizzle(SWAP,16)
	v_and_b32_e32 v86, 0x7ff8, v61
	v_add_u32_e32 v86, 0xffff8000, v86
	v_mov_b32_e32 v87, -1
	v_lshl_add_u64 v[88:89], v[86:87], 0, v[44:45]
	s_waitcnt lgkmcnt(0)
	v_bfi_b32 v94, v61, v58, v62
	v_bfi_b32 v95, v61, v59, v63
	v_bfi_b32 v96, v61, v64, v58
	v_bfi_b32 v97, v61, v65, v59
	global_store_dwordx4 v[88:89], v[94:97], off sc1
	s_nop 1
	v_lshl_add_u64 v[44:45], v[134:135], 0, s[34:35]
	s_mov_b64 s[34:35], 0x18000
	v_min_f32_e32 v78, 0x44e00000, v78
	v_min_f32_e32 v79, 0x44e00000, v79
	v_min_f32_e32 v80, 0x44e00000, v80
	v_min_f32_e32 v81, 0x44e00000, v81
	v_pk_mul_f32 v[46:47], v[78:79], s[100:101] op_sel_hi:[1,0]
	v_pk_mul_f32 v[48:49], v[80:81], s[100:101] op_sel_hi:[1,0]
	v_exp_f32_e32 v46, v46
	v_exp_f32_e32 v47, v47
	v_exp_f32_e32 v48, v48
	v_exp_f32_e32 v49, v49
	v_med3_f32 v172, v172, s81, v139
	v_med3_f32 v173, v173, s81, v139
	v_med3_f32 v174, v174, s81, v139
	v_med3_f32 v175, v175, s81, v139
	v_pk_add_f32 v[172:173], v[172:173], v[50:51]
	v_pk_add_f32 v[174:175], v[174:175], v[50:51]
	v_pk_add_f32 v[46:47], v[46:47], 1.0 op_sel_hi:[1,0]
	v_pk_add_f32 v[48:49], v[48:49], 1.0 op_sel_hi:[1,0]
	v_rcp_f32_e32 v46, v46
	v_rcp_f32_e32 v47, v47
	v_rcp_f32_e32 v48, v48
	v_rcp_f32_e32 v49, v49
	v_pk_mul_f32 v[78:79], v[78:79], s[100:101] op_sel:[0,1]
	v_pk_mul_f32 v[80:81], v[80:81], s[100:101] op_sel:[0,1]
	v_pk_mul_f32 v[78:79], v[78:79], v[46:47]
	v_pk_mul_f32 v[80:81], v[80:81], v[48:49]
	v_pk_mul_f32 v[78:79], v[78:79], v[172:173]
	v_pk_mul_f32 v[80:81], v[80:81], v[174:175]
	v_min_f32_e32 v74, 0x44e00000, v74
	v_min_f32_e32 v75, 0x44e00000, v75
	v_min_f32_e32 v76, 0x44e00000, v76
	v_min_f32_e32 v77, 0x44e00000, v77
	v_pk_mul_f32 v[46:47], v[74:75], s[100:101] op_sel_hi:[1,0]
	v_pk_mul_f32 v[48:49], v[76:77], s[100:101] op_sel_hi:[1,0]
	v_exp_f32_e32 v46, v46
	v_exp_f32_e32 v47, v47
	v_exp_f32_e32 v48, v48
	v_exp_f32_e32 v49, v49
	v_med3_f32 v18, v18, s81, v139
	v_med3_f32 v19, v19, s81, v139
	v_med3_f32 v20, v20, s81, v139
	v_med3_f32 v21, v21, s81, v139
	v_pk_add_f32 v[18:19], v[18:19], v[50:51]
	v_pk_add_f32 v[20:21], v[20:21], v[50:51]
	v_pk_add_f32 v[46:47], v[46:47], 1.0 op_sel_hi:[1,0]
	v_pk_add_f32 v[48:49], v[48:49], 1.0 op_sel_hi:[1,0]
	v_rcp_f32_e32 v46, v46
	v_rcp_f32_e32 v47, v47
	v_rcp_f32_e32 v48, v48
	v_rcp_f32_e32 v49, v49
	v_pk_mul_f32 v[74:75], v[74:75], s[100:101] op_sel:[0,1]
	v_pk_mul_f32 v[76:77], v[76:77], s[100:101] op_sel:[0,1]
	v_pk_mul_f32 v[74:75], v[74:75], v[46:47]
	v_pk_mul_f32 v[76:77], v[76:77], v[48:49]
	v_pk_mul_f32 v[74:75], v[74:75], v[18:19]
	v_pk_mul_f32 v[76:77], v[76:77], v[20:21]
	v_mov_b32_e32 v172, v131
	v_mov_b32_e32 v173, v131
	v_cvt_pk_fp8_f32 v172, v78, v79
	v_cvt_pk_fp8_f32 v173, v74, v75
	v_cvt_pk_fp8_f32 v172, v80, v81 op_sel:[0,0,1]
	v_cvt_pk_fp8_f32 v173, v76, v77 op_sel:[0,0,1]
	v_lshl_add_u64 v[44:45], v[134:135], 0, s[34:35]
	s_mov_b64 s[34:35], 0x48000
	v_min_f32_e32 v70, 0x44e00000, v70
	v_min_f32_e32 v71, 0x44e00000, v71
	v_min_f32_e32 v72, 0x44e00000, v72
	v_min_f32_e32 v73, 0x44e00000, v73
	v_pk_mul_f32 v[46:47], v[70:71], s[100:101] op_sel_hi:[1,0]
	v_pk_mul_f32 v[48:49], v[72:73], s[100:101] op_sel_hi:[1,0]
	v_exp_f32_e32 v46, v46
	v_exp_f32_e32 v47, v47
	v_exp_f32_e32 v48, v48
	v_exp_f32_e32 v49, v49
	v_med3_f32 v6, v6, s81, v139
	v_med3_f32 v7, v7, s81, v139
	v_med3_f32 v8, v8, s81, v139
	v_med3_f32 v9, v9, s81, v139
	v_pk_add_f32 v[6:7], v[6:7], v[50:51]
	v_pk_add_f32 v[8:9], v[8:9], v[50:51]
	v_pk_add_f32 v[46:47], v[46:47], 1.0 op_sel_hi:[1,0]
	v_pk_add_f32 v[48:49], v[48:49], 1.0 op_sel_hi:[1,0]
	v_rcp_f32_e32 v46, v46
	v_rcp_f32_e32 v47, v47
	v_rcp_f32_e32 v48, v48
	v_rcp_f32_e32 v49, v49
	v_pk_mul_f32 v[70:71], v[70:71], s[100:101] op_sel:[0,1]
	v_pk_mul_f32 v[72:73], v[72:73], s[100:101] op_sel:[0,1]
	v_pk_mul_f32 v[70:71], v[70:71], v[46:47]
	v_pk_mul_f32 v[72:73], v[72:73], v[48:49]
	v_pk_mul_f32 v[70:71], v[70:71], v[6:7]
	v_pk_mul_f32 v[72:73], v[72:73], v[8:9]
	v_min_f32_e32 v66, 0x44e00000, v66
	v_min_f32_e32 v67, 0x44e00000, v67
	v_min_f32_e32 v68, 0x44e00000, v68
	v_min_f32_e32 v69, 0x44e00000, v69
	v_pk_mul_f32 v[46:47], v[66:67], s[100:101] op_sel_hi:[1,0]
	v_pk_mul_f32 v[48:49], v[68:69], s[100:101] op_sel_hi:[1,0]
	v_exp_f32_e32 v46, v46
	v_exp_f32_e32 v47, v47
	v_exp_f32_e32 v48, v48
	v_exp_f32_e32 v49, v49
	v_med3_f32 v14, v14, s81, v139
	v_med3_f32 v15, v15, s81, v139
	v_med3_f32 v16, v16, s81, v139
	v_med3_f32 v17, v17, s81, v139
	v_pk_add_f32 v[14:15], v[14:15], v[50:51]
	v_pk_add_f32 v[16:17], v[16:17], v[50:51]
	v_pk_add_f32 v[46:47], v[46:47], 1.0 op_sel_hi:[1,0]
	v_pk_add_f32 v[48:49], v[48:49], 1.0 op_sel_hi:[1,0]
	v_rcp_f32_e32 v46, v46
	v_rcp_f32_e32 v47, v47
	v_rcp_f32_e32 v48, v48
	v_rcp_f32_e32 v49, v49
	v_pk_mul_f32 v[66:67], v[66:67], s[100:101] op_sel:[0,1]
	v_pk_mul_f32 v[68:69], v[68:69], s[100:101] op_sel:[0,1]
	v_pk_mul_f32 v[66:67], v[66:67], v[46:47]
	v_pk_mul_f32 v[68:69], v[68:69], v[48:49]
	v_pk_mul_f32 v[66:67], v[66:67], v[14:15]
	v_pk_mul_f32 v[68:69], v[68:69], v[16:17]
	v_mov_b32_e32 v174, v131
	v_mov_b32_e32 v175, v131
	v_cvt_pk_fp8_f32 v174, v70, v71
	v_cvt_pk_fp8_f32 v175, v66, v67
	v_cvt_pk_fp8_f32 v174, v72, v73 op_sel:[0,0,1]
	v_cvt_pk_fp8_f32 v175, v68, v69 op_sel:[0,0,1]
	v_mbcnt_lo_u32_b32 v20, -1, 0
	v_mbcnt_hi_u32_b32 v20, -1, v20
	v_bfe_i32 v21, v20, 4, 1
	v_bfi_b32 v18, v21, v172, v174
	v_bfi_b32 v19, v21, v173, v175
	ds_swizzle_b32 v18, v18 offset:swizzle(SWAP,16)
	ds_swizzle_b32 v19, v19 offset:swizzle(SWAP,16)
	v_and_b32_e32 v70, 0x7ff8, v21
	v_add_u32_e32 v70, 0xffff8000, v70
	v_mov_b32_e32 v71, -1
	v_lshl_add_u64 v[72:73], v[70:71], 0, v[44:45]
	s_waitcnt lgkmcnt(0)
	v_bfi_b32 v78, v21, v18, v172
	v_bfi_b32 v79, v21, v19, v173
	v_bfi_b32 v80, v21, v174, v18
	v_bfi_b32 v81, v21, v175, v19
	global_store_dwordx4 v[72:73], v[78:81], off sc1
	s_nop 1
	v_lshl_add_u64 v[44:45], v[134:135], 0, s[18:19]
	v_min_f32_e32 v38, 0x44e00000, v38
	v_min_f32_e32 v39, 0x44e00000, v39
	v_min_f32_e32 v40, 0x44e00000, v40
	v_min_f32_e32 v41, 0x44e00000, v41
	v_pk_mul_f32 v[46:47], v[38:39], s[100:101] op_sel_hi:[1,0]
	v_pk_mul_f32 v[48:49], v[40:41], s[100:101] op_sel_hi:[1,0]
	v_exp_f32_e32 v46, v46
	v_exp_f32_e32 v47, v47
	v_exp_f32_e32 v48, v48
	v_exp_f32_e32 v49, v49
	v_med3_f32 v98, v98, s81, v139
	v_med3_f32 v99, v99, s81, v139
	v_med3_f32 v100, v100, s81, v139
	v_med3_f32 v101, v101, s81, v139
	v_pk_add_f32 v[98:99], v[98:99], v[50:51]
	v_pk_add_f32 v[100:101], v[100:101], v[50:51]
	v_pk_add_f32 v[46:47], v[46:47], 1.0 op_sel_hi:[1,0]
	v_pk_add_f32 v[48:49], v[48:49], 1.0 op_sel_hi:[1,0]
	v_rcp_f32_e32 v46, v46
	v_rcp_f32_e32 v47, v47
	v_rcp_f32_e32 v48, v48
	v_rcp_f32_e32 v49, v49
	v_pk_mul_f32 v[38:39], v[38:39], s[100:101] op_sel:[0,1]
	v_pk_mul_f32 v[40:41], v[40:41], s[100:101] op_sel:[0,1]
	v_pk_mul_f32 v[38:39], v[38:39], v[46:47]
	v_pk_mul_f32 v[40:41], v[40:41], v[48:49]
	v_pk_mul_f32 v[38:39], v[38:39], v[98:99]
	v_pk_mul_f32 v[40:41], v[40:41], v[100:101]
	v_min_f32_e32 v34, 0x44e00000, v34
	v_min_f32_e32 v35, 0x44e00000, v35
	v_min_f32_e32 v36, 0x44e00000, v36
	v_min_f32_e32 v37, 0x44e00000, v37
	v_pk_mul_f32 v[46:47], v[34:35], s[100:101] op_sel_hi:[1,0]
	v_pk_mul_f32 v[48:49], v[36:37], s[100:101] op_sel_hi:[1,0]
	v_exp_f32_e32 v46, v46
	v_exp_f32_e32 v47, v47
	v_exp_f32_e32 v48, v48
	v_exp_f32_e32 v49, v49
	v_med3_f32 v102, v102, s81, v139
	v_med3_f32 v103, v103, s81, v139
	v_med3_f32 v104, v104, s81, v139
	v_med3_f32 v105, v105, s81, v139
	v_pk_add_f32 v[102:103], v[102:103], v[50:51]
	v_pk_add_f32 v[104:105], v[104:105], v[50:51]
	v_pk_add_f32 v[46:47], v[46:47], 1.0 op_sel_hi:[1,0]
	v_pk_add_f32 v[48:49], v[48:49], 1.0 op_sel_hi:[1,0]
	v_rcp_f32_e32 v46, v46
	v_rcp_f32_e32 v47, v47
	v_rcp_f32_e32 v48, v48
	v_rcp_f32_e32 v49, v49
	v_pk_mul_f32 v[34:35], v[34:35], s[100:101] op_sel:[0,1]
	v_pk_mul_f32 v[36:37], v[36:37], s[100:101] op_sel:[0,1]
	v_pk_mul_f32 v[34:35], v[34:35], v[46:47]
	v_pk_mul_f32 v[36:37], v[36:37], v[48:49]
	v_pk_mul_f32 v[34:35], v[34:35], v[102:103]
	v_pk_mul_f32 v[36:37], v[36:37], v[104:105]
	v_mov_b32_e32 v98, v131
	v_mov_b32_e32 v99, v131
	v_cvt_pk_fp8_f32 v98, v38, v39
	v_cvt_pk_fp8_f32 v99, v34, v35
	v_cvt_pk_fp8_f32 v98, v40, v41 op_sel:[0,0,1]
	v_cvt_pk_fp8_f32 v99, v36, v37 op_sel:[0,0,1]
	v_lshl_add_u64 v[44:45], v[134:135], 0, s[34:35]
	s_mov_b64 s[34:35], 0x50000
	v_min_f32_e32 v30, 0x44e00000, v30
	v_min_f32_e32 v31, 0x44e00000, v31
	v_min_f32_e32 v32, 0x44e00000, v32
	v_min_f32_e32 v33, 0x44e00000, v33
	v_pk_mul_f32 v[46:47], v[30:31], s[100:101] op_sel_hi:[1,0]
	v_pk_mul_f32 v[48:49], v[32:33], s[100:101] op_sel_hi:[1,0]
	v_exp_f32_e32 v46, v46
	v_exp_f32_e32 v47, v47
	v_exp_f32_e32 v48, v48
	v_exp_f32_e32 v49, v49
	v_med3_f32 v106, v106, s81, v139
	v_med3_f32 v107, v107, s81, v139
	v_med3_f32 v108, v108, s81, v139
	v_med3_f32 v109, v109, s81, v139
	v_pk_add_f32 v[106:107], v[106:107], v[50:51]
	v_pk_add_f32 v[108:109], v[108:109], v[50:51]
	v_pk_add_f32 v[46:47], v[46:47], 1.0 op_sel_hi:[1,0]
	v_pk_add_f32 v[48:49], v[48:49], 1.0 op_sel_hi:[1,0]
	v_rcp_f32_e32 v46, v46
	v_rcp_f32_e32 v47, v47
	v_rcp_f32_e32 v48, v48
	v_rcp_f32_e32 v49, v49
	v_pk_mul_f32 v[30:31], v[30:31], s[100:101] op_sel:[0,1]
	v_pk_mul_f32 v[32:33], v[32:33], s[100:101] op_sel:[0,1]
	v_pk_mul_f32 v[30:31], v[30:31], v[46:47]
	v_pk_mul_f32 v[32:33], v[32:33], v[48:49]
	v_pk_mul_f32 v[30:31], v[30:31], v[106:107]
	v_pk_mul_f32 v[32:33], v[32:33], v[108:109]
	v_min_f32_e32 v26, 0x44e00000, v26
	v_min_f32_e32 v27, 0x44e00000, v27
	v_min_f32_e32 v28, 0x44e00000, v28
	v_min_f32_e32 v29, 0x44e00000, v29
	v_pk_mul_f32 v[46:47], v[26:27], s[100:101] op_sel_hi:[1,0]
	v_pk_mul_f32 v[48:49], v[28:29], s[100:101] op_sel_hi:[1,0]
	v_exp_f32_e32 v46, v46
	v_exp_f32_e32 v47, v47
	v_exp_f32_e32 v48, v48
	v_exp_f32_e32 v49, v49
	v_med3_f32 v110, v110, s81, v139
	v_med3_f32 v111, v111, s81, v139
	v_med3_f32 v112, v112, s81, v139
	v_med3_f32 v113, v113, s81, v139
	v_pk_add_f32 v[110:111], v[110:111], v[50:51]
	v_pk_add_f32 v[112:113], v[112:113], v[50:51]
	v_pk_add_f32 v[46:47], v[46:47], 1.0 op_sel_hi:[1,0]
	v_pk_add_f32 v[48:49], v[48:49], 1.0 op_sel_hi:[1,0]
	v_rcp_f32_e32 v46, v46
	v_rcp_f32_e32 v47, v47
	v_rcp_f32_e32 v48, v48
	v_rcp_f32_e32 v49, v49
	v_pk_mul_f32 v[26:27], v[26:27], s[100:101] op_sel:[0,1]
	v_pk_mul_f32 v[28:29], v[28:29], s[100:101] op_sel:[0,1]
	v_pk_mul_f32 v[26:27], v[26:27], v[46:47]
	v_pk_mul_f32 v[28:29], v[28:29], v[48:49]
	v_pk_mul_f32 v[26:27], v[26:27], v[110:111]
	v_pk_mul_f32 v[28:29], v[28:29], v[112:113]
	v_mov_b32_e32 v100, v131
	v_mov_b32_e32 v101, v131
	v_cvt_pk_fp8_f32 v100, v30, v31
	v_cvt_pk_fp8_f32 v101, v26, v27
	v_cvt_pk_fp8_f32 v100, v32, v33 op_sel:[0,0,1]
	v_cvt_pk_fp8_f32 v101, v28, v29 op_sel:[0,0,1]
	v_mbcnt_lo_u32_b32 v104, -1, 0
	v_mbcnt_hi_u32_b32 v104, -1, v104
	v_bfe_i32 v105, v104, 4, 1
	v_bfi_b32 v102, v105, v98, v100
	v_bfi_b32 v103, v105, v99, v101
	ds_swizzle_b32 v102, v102 offset:swizzle(SWAP,16)
	ds_swizzle_b32 v103, v103 offset:swizzle(SWAP,16)
	v_and_b32_e32 v30, 0x7ff8, v105
	v_add_u32_e32 v30, 0xffff8000, v30
	v_mov_b32_e32 v31, -1
	v_lshl_add_u64 v[32:33], v[30:31], 0, v[44:45]
	s_waitcnt lgkmcnt(0)
	v_bfi_b32 v38, v105, v102, v98
	v_bfi_b32 v39, v105, v103, v99
	v_bfi_b32 v40, v105, v100, v102
	v_bfi_b32 v41, v105, v101, v103
	global_store_dwordx4 v[32:33], v[38:41], off sc1
	s_nop 1
	v_lshl_add_u64 v[44:45], v[134:135], 0, s[34:35]
	s_mov_b64 s[34:35], 0x58000
	v_min_f32_e32 v22, 0x44e00000, v22
	v_min_f32_e32 v23, 0x44e00000, v23
	v_min_f32_e32 v24, 0x44e00000, v24
	v_min_f32_e32 v25, 0x44e00000, v25
	v_pk_mul_f32 v[46:47], v[22:23], s[100:101] op_sel_hi:[1,0]
	v_pk_mul_f32 v[48:49], v[24:25], s[100:101] op_sel_hi:[1,0]
	v_exp_f32_e32 v46, v46
	v_exp_f32_e32 v47, v47
	v_exp_f32_e32 v48, v48
	v_exp_f32_e32 v49, v49
	v_med3_f32 v114, v114, s81, v139
	v_med3_f32 v115, v115, s81, v139
	v_med3_f32 v116, v116, s81, v139
	v_med3_f32 v117, v117, s81, v139
	v_pk_add_f32 v[114:115], v[114:115], v[50:51]
	v_pk_add_f32 v[116:117], v[116:117], v[50:51]
	v_pk_add_f32 v[46:47], v[46:47], 1.0 op_sel_hi:[1,0]
	v_pk_add_f32 v[48:49], v[48:49], 1.0 op_sel_hi:[1,0]
	v_rcp_f32_e32 v46, v46
	v_rcp_f32_e32 v47, v47
	v_rcp_f32_e32 v48, v48
	v_rcp_f32_e32 v49, v49
	v_pk_mul_f32 v[22:23], v[22:23], s[100:101] op_sel:[0,1]
	v_pk_mul_f32 v[24:25], v[24:25], s[100:101] op_sel:[0,1]
	v_pk_mul_f32 v[22:23], v[22:23], v[46:47]
	v_pk_mul_f32 v[24:25], v[24:25], v[48:49]
	v_pk_mul_f32 v[22:23], v[22:23], v[114:115]
	v_pk_mul_f32 v[24:25], v[24:25], v[116:117]
	v_min_f32_e32 v220, 0x44e00000, v220
	v_min_f32_e32 v221, 0x44e00000, v221
	v_min_f32_e32 v222, 0x44e00000, v222
	v_min_f32_e32 v223, 0x44e00000, v223
	v_pk_mul_f32 v[46:47], v[220:221], s[100:101] op_sel_hi:[1,0]
	v_pk_mul_f32 v[48:49], v[222:223], s[100:101] op_sel_hi:[1,0]
	v_exp_f32_e32 v46, v46
	v_exp_f32_e32 v47, v47
	v_exp_f32_e32 v48, v48
	v_exp_f32_e32 v49, v49
	v_med3_f32 v118, v118, s81, v139
	v_med3_f32 v119, v119, s81, v139
	v_med3_f32 v120, v120, s81, v139
	v_med3_f32 v121, v121, s81, v139
	v_pk_add_f32 v[118:119], v[118:119], v[50:51]
	v_pk_add_f32 v[120:121], v[120:121], v[50:51]
	v_pk_add_f32 v[46:47], v[46:47], 1.0 op_sel_hi:[1,0]
	v_pk_add_f32 v[48:49], v[48:49], 1.0 op_sel_hi:[1,0]
	v_rcp_f32_e32 v46, v46
	v_rcp_f32_e32 v47, v47
	v_rcp_f32_e32 v48, v48
	v_rcp_f32_e32 v49, v49
	v_pk_mul_f32 v[220:221], v[220:221], s[100:101] op_sel:[0,1]
	v_pk_mul_f32 v[222:223], v[222:223], s[100:101] op_sel:[0,1]
	v_pk_mul_f32 v[220:221], v[220:221], v[46:47]
	v_pk_mul_f32 v[222:223], v[222:223], v[48:49]
	v_pk_mul_f32 v[220:221], v[220:221], v[118:119]
	v_pk_mul_f32 v[222:223], v[222:223], v[120:121]
	v_mov_b32_e32 v114, v131
	v_mov_b32_e32 v115, v131
	v_cvt_pk_fp8_f32 v114, v22, v23
	v_cvt_pk_fp8_f32 v115, v220, v221
	v_cvt_pk_fp8_f32 v114, v24, v25 op_sel:[0,0,1]
	v_cvt_pk_fp8_f32 v115, v222, v223 op_sel:[0,0,1]
	v_lshl_add_u64 v[44:45], v[134:135], 0, s[34:35]
	v_min_f32_e32 v2, 0x44e00000, v2
	v_min_f32_e32 v3, 0x44e00000, v3
	v_min_f32_e32 v4, 0x44e00000, v4
	v_min_f32_e32 v5, 0x44e00000, v5
	v_pk_mul_f32 v[46:47], v[2:3], s[100:101] op_sel_hi:[1,0]
	v_pk_mul_f32 v[48:49], v[4:5], s[100:101] op_sel_hi:[1,0]
	v_exp_f32_e32 v46, v46
	v_exp_f32_e32 v47, v47
	v_exp_f32_e32 v48, v48
	v_exp_f32_e32 v49, v49
	v_med3_f32 v122, v122, s81, v139
	v_med3_f32 v123, v123, s81, v139
	v_med3_f32 v124, v124, s81, v139
	v_med3_f32 v125, v125, s81, v139
	v_pk_add_f32 v[122:123], v[122:123], v[50:51]
	v_pk_add_f32 v[124:125], v[124:125], v[50:51]
	v_pk_add_f32 v[46:47], v[46:47], 1.0 op_sel_hi:[1,0]
	v_pk_add_f32 v[48:49], v[48:49], 1.0 op_sel_hi:[1,0]
	v_rcp_f32_e32 v46, v46
	v_rcp_f32_e32 v47, v47
	v_rcp_f32_e32 v48, v48
	v_rcp_f32_e32 v49, v49
	v_pk_mul_f32 v[2:3], v[2:3], s[100:101] op_sel:[0,1]
	v_pk_mul_f32 v[4:5], v[4:5], s[100:101] op_sel:[0,1]
	v_pk_mul_f32 v[2:3], v[2:3], v[46:47]
	v_pk_mul_f32 v[4:5], v[4:5], v[48:49]
	v_pk_mul_f32 v[2:3], v[2:3], v[122:123]
	v_pk_mul_f32 v[4:5], v[4:5], v[124:125]
	v_min_f32_e32 v10, 0x44e00000, v10
	v_min_f32_e32 v11, 0x44e00000, v11
	v_min_f32_e32 v12, 0x44e00000, v12
	v_min_f32_e32 v13, 0x44e00000, v13
	v_pk_mul_f32 v[46:47], v[10:11], s[100:101] op_sel_hi:[1,0]
	v_pk_mul_f32 v[48:49], v[12:13], s[100:101] op_sel_hi:[1,0]
	v_exp_f32_e32 v46, v46
	v_exp_f32_e32 v47, v47
	v_exp_f32_e32 v48, v48
	v_exp_f32_e32 v49, v49
	v_med3_f32 v126, v126, s81, v139
	v_med3_f32 v127, v127, s81, v139
	v_med3_f32 v128, v128, s81, v139
	v_med3_f32 v129, v129, s81, v139
	v_pk_add_f32 v[126:127], v[126:127], v[50:51]
	v_pk_add_f32 v[128:129], v[128:129], v[50:51]
	v_pk_add_f32 v[46:47], v[46:47], 1.0 op_sel_hi:[1,0]
	v_pk_add_f32 v[48:49], v[48:49], 1.0 op_sel_hi:[1,0]
	v_rcp_f32_e32 v46, v46
	v_rcp_f32_e32 v47, v47
	v_rcp_f32_e32 v48, v48
	v_rcp_f32_e32 v49, v49
	v_pk_mul_f32 v[10:11], v[10:11], s[100:101] op_sel:[0,1]
	v_pk_mul_f32 v[12:13], v[12:13], s[100:101] op_sel:[0,1]
	v_pk_mul_f32 v[10:11], v[10:11], v[46:47]
	v_pk_mul_f32 v[12:13], v[12:13], v[48:49]
	v_pk_mul_f32 v[10:11], v[10:11], v[126:127]
	v_pk_mul_f32 v[12:13], v[12:13], v[128:129]
	v_mov_b32_e32 v116, v131
	v_mov_b32_e32 v117, v131
	v_cvt_pk_fp8_f32 v116, v2, v3
	v_cvt_pk_fp8_f32 v117, v10, v11
	v_cvt_pk_fp8_f32 v116, v4, v5 op_sel:[0,0,1]
	v_cvt_pk_fp8_f32 v117, v12, v13 op_sel:[0,0,1]
	v_mbcnt_lo_u32_b32 v120, -1, 0
	v_mbcnt_hi_u32_b32 v120, -1, v120
	v_bfe_i32 v121, v120, 4, 1
	v_bfi_b32 v118, v121, v114, v116
	v_bfi_b32 v119, v121, v115, v117
	ds_swizzle_b32 v118, v118 offset:swizzle(SWAP,16)
	ds_swizzle_b32 v119, v119 offset:swizzle(SWAP,16)
	v_and_b32_e32 v2, 0x7ff8, v121
	v_add_u32_e32 v2, 0xffff8000, v2
	v_mov_b32_e32 v3, -1
	v_lshl_add_u64 v[4:5], v[2:3], 0, v[44:45]
	s_waitcnt lgkmcnt(0)
	v_bfi_b32 v22, v121, v118, v114
	v_bfi_b32 v23, v121, v119, v115
	v_bfi_b32 v24, v121, v116, v118
	v_bfi_b32 v25, v121, v117, v119
	global_store_dwordx4 v[4:5], v[22:25], off sc1
	s_nop 1
	s_cbranch_vccnz .LBB0_1269
	v_readlane_b32 s88, v254, 4
	s_ashr_i32 s45, s44, 31
	v_readlane_b32 s92, v254, 8
	v_readlane_b32 s93, v254, 9
	s_lshl_b64 s[4:5], s[44:45], 14
	s_mov_b64 s[56:57], s[92:93]
	s_add_u32 s22, s56, s4
	v_mov_b32_e32 v2, v131
	s_addc_u32 s34, s57, s5
	s_lshl_b32 s4, s46, 7
	s_ashr_i32 s5, s4, 31
	v_mbcnt_lo_u32_b32 v2, -1, v2
	s_lshl_b64 s[4:5], s[4:5], 2
	v_mbcnt_hi_u32_b32 v2, -1, v2
	s_add_u32 s4, s22, s4
	s_addc_u32 s5, s34, s5
	s_lshl_b32 s22, s63, 2
	v_ashrrev_i32_e32 v2, 1, v2
	s_add_u32 s4, s4, s22
	v_and_b32_e32 v2, -8, v2
	s_addc_u32 s5, s5, 0
	v_ashrrev_i32_e32 v3, 31, v2
	v_lshl_add_u64 v[6:7], v[2:3], 2, s[4:5]
	v_lshl_add_u64 v[14:15], v[6:7], 0, s[6:7]
	global_load_dwordx4 v[10:13], v[6:7], off offset:16
	global_load_dwordx4 v[2:5], v[6:7], off
	v_add_co_u32_e32 v6, vcc, 0x2000, v6
	v_readlane_b32 s89, v254, 5
	s_nop 0
	v_addc_co_u32_e32 v7, vcc, 0, v7, vcc
	global_load_dwordx4 v[6:9], v[6:7], off
	s_nop 0
	global_load_dwordx4 v[14:17], v[14:15], off offset:16
	s_andn2_b64 vcc, exec, s[24:25]
	v_readlane_b32 s90, v254, 6
	v_readlane_b32 s91, v254, 7
	v_readlane_b32 s94, v254, 10
	v_readlane_b32 s95, v254, 11
	s_cbranch_vccnz .LBB0_1268
	s_barrier
